# p_mix: 48 instead of 96 workgroups start with next-layer weight-conversion tickets (ticket loop unchanged, any workgroup still drains what is left), on top of the K-loop peel
# baseline (speedup 1.0000x reference)
.LBB0_511:
	v_readlane_b32 s0, v254, 9
	s_mov_b32 s1, -1
	s_nop 0
	v_mbcnt_lo_u32_b32 v0, s1, 0
	v_mbcnt_hi_u32_b32 v0, s1, v0
	v_lshl_add_u32 v186, s0, 6, v0
	v_readlane_b32 s0, v254, 53
	v_readlane_b32 s1, v254, 54
	s_lshl_b32 s26, s0, 6
	s_mov_b32 s2, s0
	s_lshl_b64 s[4:5], s[26:27], 2
	v_readlane_b32 s0, v255, 0
	v_readlane_b32 s1, v255, 1
	s_add_u32 s0, s0, s4
	v_writelane_b32 v255, s4, 8
	s_addc_u32 s1, s1, s5
	s_add_u32 s0, s0, 0x9000
	v_writelane_b32 v255, s5, 9
	s_addc_u32 s1, s1, 0
	s_add_i32 s4, s2, 1
	v_writelane_b32 v255, s0, 10
	s_cmp_lg_u32 s2, 3
	s_cselect_b64 s[2:3], -1, 0
	v_writelane_b32 v255, s1, 11
	s_sub_i32 s0, s14, 64
	s_cmpk_lt_u32 s0, 0x30
	v_writelane_b32 v255, s2, 12
	s_cselect_b64 s[0:1], -1, 0
	v_cmp_eq_u32_e64 s[36:37], 0, v186
	v_writelane_b32 v255, s3, 13
	v_writelane_b32 v255, s0, 14
	s_nop 1
	v_writelane_b32 v255, s1, 15
	s_and_b64 s[0:1], s[2:3], s[0:1]
	s_andn2_b64 vcc, exec, s[0:1]
	s_mul_hi_u32 s0, s4, 0xbd00000
	v_writelane_b32 v255, s0, 16
	s_mul_i32 s0, s4, 0xbd00000
	v_writelane_b32 v255, s0, 17
	s_mul_hi_u32 s0, s4, 0x2b00000
	v_writelane_b32 v255, s0, 18
	s_mul_i32 s0, s4, 0x2b00000
	v_writelane_b32 v255, s0, 19
	s_mul_hi_u32 s0, s4, 0x5600000
	v_writelane_b32 v255, s0, 20
	s_mul_i32 s0, s4, 0x5600000
	v_writelane_b32 v255, s0, 21
	s_mul_hi_u32 s0, s4, 0x4ea0000
	v_writelane_b32 v255, s0, 22
	s_mov_b32 s0, s4
	v_writelane_b32 v255, s0, 23
	s_nop 1
	v_writelane_b32 v255, s1, 24
	s_mul_i32 s0, s4, 0x4ea0000
	v_writelane_b32 v255, s0, 25
	s_cbranch_vccnz .LBB0_701
	v_readlane_b32 s0, v254, 44
	s_add_i32 s20, s47, s0
	v_readlane_b32 s0, v255, 2
	v_readlane_b32 s1, v255, 17
	s_add_u32 s21, s0, s1
	v_readlane_b32 s0, v255, 4
	v_readlane_b32 s1, v255, 16
	s_addc_u32 s31, s0, s1
	s_add_u32 s34, s21, 0xa780000
	v_readlane_b32 s0, v254, 46
	s_addc_u32 s35, s31, 0
	s_lshl_b32 s0, s0, 1
	v_readlane_b32 s6, v255, 23
	s_add_u32 s38, s34, s0
	v_readlane_b32 s7, v255, 24
	s_addc_u32 s39, s35, 0
	s_mov_b32 s7, s27
	s_add_u32 s40, s21, 0x7c80000
	s_addc_u32 s41, s31, 0
	s_lshl_b64 s[2:3], s[6:7], 13
	s_lshl_b64 s[4:5], s[6:7], 24
	s_add_u32 s42, s21, 0x7480000
	s_addc_u32 s43, s31, 0
	s_mov_b32 s0, s6
	s_lshl_b64 s[6:7], s[6:7], 23
	s_add_u32 s44, s21, 0x7080000
	s_addc_u32 s45, s31, 0
	s_add_u32 s46, s21, 0x6880000
	s_addc_u32 s47, s31, 0
	s_add_u32 s48, s21, 0x4080000
	s_addc_u32 s49, s31, 0
	v_writelane_b32 v255, s0, 23
	s_add_u32 s50, s21, 0x2b00000
	s_addc_u32 s51, s31, 0
	v_writelane_b32 v255, s1, 24
	s_branch .LBB0_515
